# P7b epilogue x-load ring + P2 GEMM workgroups 160->168 (16 rounds instead of 17)
# baseline (speedup 1.0000x reference)
; #define PH_BEGIN ArgsC* A = args_ptr(); unsigned char* const ws = A->ws; (void)ws
; #define Q_LOAD() do { _Pragma("unroll") for (int g = 0; g < 8; ++g) _Pragma("unroll") for (int r = 0; r < 4; ++r) v[g][r] = __builtin_nontemporal_load((const f32x4*)(Wp + (size_t)(256 * g + 32 * wave + 4 * kr + r) * ldw + 4 * n4)); } while (0)
; #define Q_GRAB() (((stop != nullptr && xb_ld(stop) >= thr) || (quota > 0 && qleft-- <= 0)) ? (unsigned)hi : (unsigned)lo + atomicAdd(cnt, 1u))
;     ...
;     __syncthreads();
;     if (tid == 0) MISC[2] = Q_GRAB();
;     __syncthreads();
;     int cur = (int)MISC[2];
;     __syncthreads();
;     if (cur < hi) { Q_ITEM(cur); Q_LOAD(); }
; __global__ void __launch_bounds__(NWAVES * 64, 2) fwd_kernel(Args a_unused) {
;     ...
;     if (IN(2)) {
;         PH_BEGIN;
;         constexpr int GA = 160, NUN = (MROWS / 256) * (INC / 256);
;         const int Gact = (G == 256) ? GA : G;
;         if (bx >= Gact) {
;             quant_queue(A, ws, ctl, lds, MISC, ctl + CW_QE, QN0, QN0 + 6144, ctl + CW_DONE, (unsigned)((NUN % GA) ? GA - NUN % GA + 1 : 1));
;         } else {
;         pg8::Gemm g{H, WIN, D / 2}; pg8::PlainOrder S; S.init(MROWS / 256, INC / 256, Gact, bx); S.K2 = D;
;         EpiProj E{PROJ, lbf, lbb, (const float*)(ws + WS_CS + CS_HROW), (const float*)(ws + WS_CS + CS_WIN)};
;         { const unsigned long long t0_ = __builtin_amdgcn_s_memrealtime(); const unsigned long long dl_ = (unsigned long long)(vcu & 7) * (STAG_TICKS / 2);
;           while (__builtin_amdgcn_s_memrealtime() - t0_ < dl_) __builtin_amdgcn_s_sleep(4); }
;         pg8::gemm_phase<EpiProj, pg8::PlainOrder, true>(lds, g, S, E);
;         if (tid == 0) atomicAdd(ctl + CW_DONE, 1u);
;         }
.LBB0_302:
	s_cmp_lt_i32 s46, 3
	s_cselect_b64 s[6:7], -1, 0
	s_and_b64 s[14:15], s[6:7], s[4:5]
	s_andn2_b64 vcc, exec, s[14:15]
	s_cbranch_vccnz .LBB0_1126
	s_mov_b64 s[18:19], s[0:1]
	s_load_dwordx2 s[16:17], s[18:19], 0xc8
	s_cmpk_lg_i32 s33, 0x100
	s_cselect_b32 s57, s33, 0xa8
	s_cmp_lt_i32 s2, s57
	s_mov_b64 s[4:5], -1
	s_cbranch_scc1 .LBB0_446
	s_add_u32 s20, s48, 0x9100
	s_addc_u32 s21, s49, 0
	s_add_u32 s22, s48, 0x9200
	s_addc_u32 s23, s49, 0
	v_readfirstlane_b32 s12, v0
	s_waitcnt lgkmcnt(0)
	s_barrier
	s_and_saveexec_b64 s[4:5], s[40:41]
	s_cbranch_execz .LBB0_310
	v_mov_b32_e32 v1, 0
	global_load_dword v1, v1, s[22:23] sc1
	s_waitcnt vmcnt(0)
	v_cmp_lt_u32_e32 vcc, 23, v1
	v_mov_b32_e32 v1, 0x19c8
	s_cbranch_vccnz .LBB0_309
	s_mov_b64 s[8:9], exec
	v_mbcnt_lo_u32_b32 v1, s8, 0
	v_mbcnt_hi_u32_b32 v1, s9, v1
	v_cmp_eq_u32_e32 vcc, 0, v1
	s_and_saveexec_b64 s[6:7], vcc
	s_cbranch_execz .LBB0_308
	s_bcnt1_i32_b64 s3, s[8:9]
	v_mov_b32_e32 v2, 0
	v_mov_b32_e32 v3, s3
	global_atomic_add v2, v2, v3, s[20:21] sc0

; #define Q_GRAB() (((stop != nullptr && xb_ld(stop) >= thr) || (quota > 0 && qleft-- <= 0)) ? (unsigned)hi : (unsigned)lo + atomicAdd(cnt, 1u))
;     ...
;     while (cur < hi) {
;         unsigned nxt = 0u; if (tid == 0) nxt = Q_GRAB();
.LBB0_334:
	v_mov_b32_e32 v1, 0
	s_and_saveexec_b64 s[6:7], s[40:41]
	s_cbranch_execz .LBB0_339
	global_load_dword v1, v171, s[22:23] sc1
	s_waitcnt vmcnt(0)
	v_cmp_lt_u32_e32 vcc, 23, v1
	v_mov_b32_e32 v1, 0x19c8
	s_cbranch_vccnz .LBB0_339
	s_mov_b64 s[34:35], exec
	v_mbcnt_lo_u32_b32 v1, s34, 0
	v_mbcnt_hi_u32_b32 v1, s35, v1
	v_cmp_eq_u32_e32 vcc, 0, v1
	s_and_saveexec_b64 s[12:13], vcc
	s_cbranch_execz .LBB0_338
	s_bcnt1_i32_b64 s34, s[34:35]
	v_mov_b32_e32 v130, s34
	global_atomic_add v130, v171, v130, s[20:21] sc0
